# v61 + attention item prologue: early vmcnt(0) removed so the second K tile is requested before Q and the first tile land
# baseline (speedup 1.0000x reference)
; #define TID() (lnd_s(wv_) * 64 + (int)__builtin_amdgcn_mbcnt_hi(~0u, __builtin_amdgcn_mbcnt_lo(~0u, (unsigned)lnd_s(0))))
; __device__ __forceinline__ int v_rd_base(int lane) { const int g = lane >> 4, c = lane & 15; return (8 * (g >> 1) + (c >> 2)) * KPITCH + (16 * (g & 1) + 4 * (c & 3)) * 2; }
; #define SLOAD(k0) do { \
;     ks0 = *(const bf16x8*)(&Kh[(long)(k0) * LDK + kg[0]]); ks1 = *(const bf16x8*)(&Kh[(long)(k0) * LDK + kg[1]]); ks2 = *(const bf16x8*)(&Kh[(long)(k0) * LDK + kg[2]]); } while (0)
; #define SWRITE(b) do { \
;     *(bf16x8*)(K_lds + (b) * SHM_K + kl[0]) = ks0; *(bf16x8*)(K_lds + (b) * SHM_K + kl[1]) = ks1; *(bf16x8*)(K_lds + (b) * SHM_K + kl[2]) = ks2; } while (0)
; #define SWAIT() asm volatile("s_waitcnt vmcnt(0)" ::: "memory")
; template <int VAR> __device__ __forceinline__ void attn_dense_body(const int wv_, const bf16_t* __restrict__ Qb, const bf16_t* __restrict__ Kh, const bf16_t* __restrict__ Vh, bf16_t* __restrict__ Ob, int seq, unsigned char* lds) {
;     const int tid = TID(), wid = tid >> 6, lane = tid & 63, r32 = lane & 31, hi = lane >> 5;
;     unsigned char* K_lds = lds;
;     float* ws = (float*)(lds + 2 * SHM_K) + wid * 64; float* li_l = ws; float* al_l = ws + 32;
;     float m_reg = -1e30f, l_reg = 0; f32x16 o[4] = {}; bf16x8 qr[12];
;     const bf16_t* Qw = Qb + (long)(wid * QBLK + r32) * LDQ + hi * 8;
; #pragma unroll
;     for (int d0 = 0; d0 < 12; ++d0) qr[d0] = *(const bf16x8*)(Qw + d0 * 16);
;     int kg[3], kl[3];
; #pragma unroll
;     for (int i = 0; i < 3; ++i) { const int id = tid + 512 * i, row = id / 24, ch = id % 24; kg[i] = row * LDK + ch * 8; kl[i] = KSWZ(row, ch * 16); }
;     const int vb0 = (int)(uintptr_t)K_lds + v_rd_base(lane);
;     bf16x8 ks0, ks1, ks2;
;     ...
;     f32x16 p0, p1; float mn, al; bf16x8 pa0, pa1, pa2, pa3; const int NT = seq / KVBLK;
;     SLOAD(0); SWAIT(); SWRITE(0); SLOAD(KVBLK);
.LBB0_998:
	v_readlane_b32 s36, v254, 5
	s_mov_b32 s37, 0
	s_lshl_b32 s0, s5, 5
	v_mbcnt_lo_u32_b32 v0, -1, s37
	v_mbcnt_hi_u32_b32 v166, -1, v0
	v_lshl_add_u32 v26, s36, 6, v166
	s_mov_b32 s37, 0x2aaaaaab
	v_mul_hi_i32 v0, v26, s37
	v_lshrrev_b32_e32 v1, 31, v0
	v_ashrrev_i32_e32 v0, 2, v0
	s_and_b32 s0, s0, 0xe0
	s_and_b32 s1, s5, 0xffffff00
	v_add_u32_e32 v27, v0, v1
	v_add_u32_e32 v1, 0x200, v26
	s_or_b32 s0, s0, s1
	s_bfe_u32 s1, s5, 0x50003
	v_mul_hi_i32 v2, v1, s37
	s_or_b32 s2, s0, s1
	v_lshrrev_b32_e32 v3, 31, v2
	v_ashrrev_i32_e32 v2, 2, v2
	s_and_b64 s[0:1], s[42:43], exec
	v_add_u32_e32 v29, v2, v3
	s_cselect_b32 s2, s2, s5
	s_movk_i32 s36, 0xc0
	v_mul_lo_u32 v2, v29, 24
	s_ashr_i32 s44, s2, 4
	v_sub_u32_e32 v30, v1, v2
	v_mul_lo_u32 v1, v29, s36
	s_ashr_i32 s46, s2, 6
	s_ashr_i32 s45, s44, 31
	s_lshl_b32 s2, s2, 8
	v_lshl_add_u32 v2, v30, 3, v1
	v_add_u32_e32 v1, 0x400, v26
	s_lshl_b64 s[0:1], s[44:45], 12
	s_and_b32 s45, s2, 0xf00
	v_mul_hi_i32 v3, v1, s37
	s_or_b32 s0, s0, s45
	v_lshrrev_b32_e32 v4, 31, v3
	v_ashrrev_i32_e32 v3, 2, v3
	s_mulk_i32 s1, 0x180
	s_mul_hi_u32 s2, s0, 0x180
	v_add_u32_e32 v31, v3, v4
	s_add_i32 s1, s2, s1
	s_mulk_i32 s0, 0x180
	v_mul_lo_u32 v0, v27, 24
	v_mul_lo_u32 v3, v31, 24
	s_add_u32 s2, s21, s0
	v_sub_u32_e32 v28, v26, v0
	v_mul_lo_u32 v0, v27, s36
	v_sub_u32_e32 v32, v1, v3
	v_mul_lo_u32 v1, v31, s36
	s_addc_u32 s3, s22, s1
	s_ashr_i32 s47, s46, 31
	s_mul_i32 s38, s46, 0x180000
	v_ashrrev_i32_e32 v170, 6, v26
	v_lshl_add_u32 v0, v28, 3, v0
	v_lshl_add_u32 v8, v32, 3, v1
	s_mul_hi_i32 s29, s46, 0x180000
	s_add_u32 s0, s23, s38
	v_and_b32_e32 v168, 31, v166
	v_lshlrev_b32_e32 v158, 5, v170
	v_ashrrev_i32_e32 v1, 31, v0
	v_ashrrev_i32_e32 v3, 31, v2
	v_ashrrev_i32_e32 v9, 31, v8
	s_addc_u32 s1, s24, s29
	v_bfe_u32 v169, v166, 5, 1
	v_lshlrev_b64 v[12:13], 1, v[0:1]
	v_lshlrev_b64 v[16:17], 1, v[2:3]
	v_lshlrev_b64 v[20:21], 1, v[8:9]
	v_or_b32_e32 v33, v158, v168
	v_mov_b64_e32 v[24:25], s[2:3]
	v_lshl_add_u64 v[14:15], s[0:1], 0, v[12:13]
	v_lshl_add_u64 v[18:19], s[0:1], 0, v[16:17]
	v_lshl_add_u64 v[22:23], s[0:1], 0, v[20:21]
	v_mad_i64_i32 v[24:25], s[0:1], v33, s28, v[24:25]
	v_lshlrev_b32_e32 v96, 4, v169
	v_lshl_add_u64 v[24:25], v[24:25], 0, v[96:97]
	global_load_dwordx4 v[0:3], v[14:15], off
	global_load_dwordx4 v[4:7], v[18:19], off
	global_load_dwordx4 v[8:11], v[22:23], off
	global_load_dwordx4 v[142:145], v[24:25], off
	global_load_dwordx4 v[138:141], v[24:25], off offset:32
	global_load_dwordx4 v[134:137], v[24:25], off offset:64
	global_load_dwordx4 v[130:133], v[24:25], off offset:96
	global_load_dwordx4 v[126:129], v[24:25], off offset:128
	global_load_dwordx4 v[122:125], v[24:25], off offset:160
	global_load_dwordx4 v[118:121], v[24:25], off offset:192
	global_load_dwordx4 v[114:117], v[24:25], off offset:224
	global_load_dwordx4 v[110:113], v[24:25], off offset:256
	global_load_dwordx4 v[106:109], v[24:25], off offset:288
	global_load_dwordx4 v[102:105], v[24:25], off offset:320
	global_load_dwordx4 v[98:101], v[24:25], off offset:352
	s_movk_i32 s0, 0x6000
	v_add_co_u32_e32 v14, vcc, s0, v14
	s_movk_i32 s1, 0x190
	s_nop 0
	v_addc_co_u32_e32 v15, vcc, 0, v15, vcc
	v_add_co_u32_e32 v18, vcc, s0, v18
	s_cmp_lg_u32 0, -1
	s_nop 0
	v_addc_co_u32_e32 v19, vcc, 0, v19, vcc
	global_load_dwordx4 v[146:149], v[14:15], off
	global_load_dwordx4 v[150:153], v[18:19], off
	v_add_co_u32_e32 v14, vcc, s0, v22
	v_lshlrev_b32_e32 v18, 2, v166
	s_nop 0
	v_addc_co_u32_e32 v15, vcc, 0, v23, vcc
	global_load_dwordx4 v[154:157], v[14:15], off
	v_and_b32_e32 v14, 0x3fffffc0, v26
	v_lshl_add_u32 v159, v14, 2, 0
	v_mul_lo_u32 v14, v27, s1
	v_lshl_add_u32 v175, v28, 4, v14
	v_mul_lo_u32 v14, v29, s1
	v_lshl_add_u32 v176, v30, 4, v14
	v_mul_lo_u32 v14, v31, s1
	v_lshl_add_u32 v177, v32, 4, v14
	v_lshrrev_b32_e32 v14, 2, v166
	v_and_b32_e32 v15, 16, v166
	v_and_b32_e32 v14, 11, v14
	v_and_or_b32 v15, v18, 12, v15
	v_add_u32_e32 v18, 0, v175
	v_mul_u32_u24_e32 v14, 0x190, v14
	v_lshlrev_b32_e32 v15, 1, v15
	v_mad_u32_u24 v178, v168, s1, v96
	s_cselect_b32 s1, 0, 0
	s_add_u32 s2, s25, s38
	v_add3_u32 v172, v14, s1, v15
	s_addc_u32 s3, s48, s29
	v_mov_b32_e32 v14, v97
	v_mov_b32_e32 v15, v97
	v_and_b32_e32 v167, 63, v166
	v_lshl_add_u64 v[160:161], s[2:3], 0, v[20:21]
	v_lshl_add_u64 v[162:163], s[2:3], 0, v[16:17]
	v_lshl_add_u64 v[164:165], s[2:3], 0, v[12:13]
	v_mov_b32_e32 v12, v97
	v_mov_b32_e32 v13, v97
	s_mov_b32 s0, 0
	v_cmp_gt_u32_e64 s[36:37], 32, v167
	v_lshl_add_u32 v171, v168, 2, v159
	v_mov_b32_e32 v179, 0
	v_mov_b32_e32 v173, 0xf149f2ca
	s_mov_b64 s[2:3], 0
	s_waitcnt vmcnt(3)
	ds_write_b128 v18, v[0:3]
	v_add_u32_e32 v0, 0, v176
	ds_write_b128 v0, v[4:7]
	v_add_u32_e32 v0, 0, v177
	ds_write_b128 v0, v[8:11]
	v_mov_b32_e32 v0, v97
	v_mov_b32_e32 v1, v97
	v_mov_b32_e32 v2, v97
	v_mov_b32_e32 v3, v97
	v_mov_b32_e32 v4, v97
	v_mov_b32_e32 v5, v97
	v_mov_b32_e32 v6, v97
	v_mov_b32_e32 v7, v97
	v_mov_b32_e32 v8, v97
	v_mov_b32_e32 v9, v97
	v_mov_b32_e32 v10, v97
	v_mov_b32_e32 v11, v97
	v_mov_b64_e32 v[62:63], v[14:15]
	v_mov_b64_e32 v[46:47], v[14:15]
	v_mov_b64_e32 v[30:31], v[14:15]
	v_mov_b64_e32 v[60:61], v[12:13]
	v_mov_b64_e32 v[58:59], v[10:11]
	v_mov_b64_e32 v[56:57], v[8:9]
	v_mov_b64_e32 v[54:55], v[6:7]
	v_mov_b64_e32 v[52:53], v[4:5]
	v_mov_b64_e32 v[50:51], v[2:3]
	v_mov_b64_e32 v[48:49], v[0:1]
	v_mov_b64_e32 v[44:45], v[12:13]
	v_mov_b64_e32 v[42:43], v[10:11]
	v_mov_b64_e32 v[40:41], v[8:9]
	v_mov_b64_e32 v[38:39], v[6:7]
	v_mov_b64_e32 v[36:37], v[4:5]
	v_mov_b64_e32 v[34:35], v[2:3]
	v_mov_b64_e32 v[32:33], v[0:1]
	v_mov_b64_e32 v[28:29], v[12:13]
	v_mov_b64_e32 v[26:27], v[10:11]
	v_mov_b64_e32 v[24:25], v[8:9]
	v_mov_b64_e32 v[22:23], v[6:7]
	v_mov_b64_e32 v[20:21], v[4:5]
	v_mov_b64_e32 v[18:19], v[2:3]
	v_mov_b64_e32 v[16:17], v[0:1]
